# speedup vs baseline: 1.0082x; 1.0082x over previous
.LBB2_110:
	s_or_b64 exec, exec, s[0:1]
	v_bfe_u32 v65, v0, 6, 1
	v_bfe_u32 v1, v0, 3, 1
	v_lshl_or_b32 v46, v65, 1, v1
	v_lshrrev_b32_e32 v1, 3, v0
	v_and_b32_e32 v97, 15, v0
	v_and_b32_e32 v1, 48, v1
	v_or_b32_e32 v63, v1, v97
	v_mul_lo_u16_e32 v2, 20, v63
	v_lshrrev_b16_e32 v2, 7, v2
	v_and_b32_e32 v2, 14, v2
	v_or_b32_e32 v110, 64, v63
	v_add_u32_sdwa v6, v63, v2 dst_sel:DWORD dst_unused:UNUSED_PAD src0_sel:DWORD src1_sel:WORD_0
	v_mul_lo_u16_e32 v2, 0x4f, v110
	v_lshrrev_b16_e32 v2, 9, v2
	v_and_b32_e32 v2, 62, v2
	v_bfe_u32 v62, v0, 4, 2
	v_and_b32_e32 v47, 7, v0
	v_add_u32_e32 v10, v110, v2
	v_lshl_add_u32 v84, v62, 4, 0
	v_mad_u32_u24 v2, v46, 10, v47
	s_movk_i32 s0, 0x110
	s_waitcnt vmcnt(0)
	v_mad_u32_u24 v34, v2, s0, v84
	s_waitcnt lgkmcnt(0)
	s_barrier
	ds_read_b128 v[2:5], v34 offset:61200
	v_or_b32_e32 v64, 0x80, v63
	v_min_u32_e32 v22, 0xa8, v64
	v_mul_lo_u16_e32 v7, 0x4f, v22
	v_mad_u32_u24 v98, v6, s0, v84
	v_lshrrev_b16_e32 v23, 9, v7
	ds_read_b128 v[6:9], v98
	v_mad_u32_u24 v111, v10, s0, v84
	ds_read_b128 v[10:13], v111
	ds_read_b128 v[14:17], v34 offset:61264
	ds_read_b128 v[18:21], v98 offset:64
	v_and_b32_e32 v23, 30, v23
	s_waitcnt lgkmcnt(3)
	v_mfma_f32_16x16x32_f16 v[6:9], v[2:5], v[6:9], 0
	v_add_u32_e32 v26, v22, v23
	v_mad_u32_u24 v117, v26, s0, v84
	ds_read_b128 v[22:25], v111 offset:64
	ds_read_b128 v[26:29], v117
	ds_read_b128 v[30:33], v117 offset:64
	s_waitcnt lgkmcnt(3)
	v_mfma_f32_16x16x32_f16 v[6:9], v[14:17], v[18:21], v[6:9]
	ds_read_b128 v[18:21], v34 offset:61328
	v_add_u32_e32 v58, 1, v47
	v_add_u32_e32 v85, 2, v47
	v_mfma_f32_16x16x32_f16 v[10:13], v[2:5], v[10:13], 0
	v_lshl_or_b32 v86, s2, 9, v0
	v_ashrrev_i32_e32 v87, 31, v86
	v_lshlrev_b64 v[74:75], 4, v[86:87]
	s_waitcnt lgkmcnt(2)
	v_mfma_f32_16x16x32_f16 v[2:5], v[2:5], v[26:29], 0
	v_mad_u32_u24 v90, v46, 10, 20
	v_lshl_add_u64 v[70:71], s[60:61], 0, v[74:75]
	v_add_co_u32_e32 v42, vcc, 0x200000, v70
	v_mfma_f32_16x16x32_f16 v[10:13], v[14:17], v[22:25], v[10:13]
	s_nop 0
	v_addc_co_u32_e32 v43, vcc, 0, v71, vcc
	v_add_co_u32_e32 v50, vcc, 0x400000, v70
	s_waitcnt lgkmcnt(1)
	v_mfma_f32_16x16x32_f16 v[2:5], v[14:17], v[30:33], v[2:5]
	ds_read_b128 v[14:17], v98 offset:128
	ds_read_b128 v[22:25], v34 offset:61392
	ds_read_b128 v[26:29], v98 offset:192
	v_addc_co_u32_e32 v51, vcc, 0, v71, vcc
	s_waitcnt lgkmcnt(2)
	v_mfma_f32_16x16x32_f16 v[6:9], v[18:21], v[14:17], v[6:9]
	ds_read_b128 v[14:17], v111 offset:128
	ds_read_b128 v[30:33], v111 offset:192
	v_add_co_u32_e32 v52, vcc, 0x600000, v70
	s_waitcnt lgkmcnt(1)
	v_mfma_f32_16x16x32_f16 v[10:13], v[18:21], v[14:17], v[10:13]
	ds_read_b128 v[14:17], v117 offset:128
	ds_read_b128 v[34:37], v117 offset:192
	v_addc_co_u32_e32 v53, vcc, 0, v71, vcc
	s_waitcnt lgkmcnt(1)
	v_mfma_f32_16x16x32_f16 v[2:5], v[18:21], v[14:17], v[2:5]
	v_mad_u32_u24 v14, v46, 10, v58
	v_mad_u32_u24 v38, v14, s0, v84
	ds_read_b128 v[14:17], v38 offset:61200
	v_mfma_f32_16x16x32_f16 v[6:9], v[22:25], v[26:29], v[6:9]
	v_add_co_u32_e32 v54, vcc, 0x800000, v70
	s_mov_b32 s1, 0x200000
	v_mfma_f32_16x16x32_f16 v[10:13], v[22:25], v[30:33], v[10:13]
	v_addc_co_u32_e32 v55, vcc, 0, v71, vcc
	v_lshl_add_u64 v[82:83], s[62:63], 0, v[74:75]
	s_waitcnt lgkmcnt(1)
	v_mfma_f32_16x16x32_f16 v[2:5], v[22:25], v[34:37], v[2:5]
	ds_read_b128 v[18:21], v98 offset:272
	ds_read_b128 v[22:25], v38 offset:61264
	ds_read_b128 v[26:29], v98 offset:336
	s_mov_b32 s2, 0x400000
	s_mov_b32 s3, 0x600000
	s_waitcnt lgkmcnt(2)
	v_mfma_f32_16x16x32_f16 v[6:9], v[14:17], v[18:21], v[6:9]
	ds_read_b128 v[18:21], v111 offset:272
	ds_read_b128 v[30:33], v111 offset:336
	s_add_i32 s6, 0, 0x13890
	s_waitcnt lgkmcnt(1)
	v_mfma_f32_16x16x32_f16 v[10:13], v[14:17], v[18:21], v[10:13]
	ds_read_b128 v[18:21], v117 offset:272
	ds_read_b128 v[34:37], v117 offset:336
	s_waitcnt lgkmcnt(1)
	v_mfma_f32_16x16x32_f16 v[2:5], v[14:17], v[18:21], v[2:5]
	ds_read_b128 v[14:17], v38 offset:61328
	v_mfma_f32_16x16x32_f16 v[6:9], v[22:25], v[26:29], v[6:9]
	v_mfma_f32_16x16x32_f16 v[10:13], v[22:25], v[30:33], v[10:13]
	s_waitcnt lgkmcnt(1)
	v_mfma_f32_16x16x32_f16 v[2:5], v[22:25], v[34:37], v[2:5]
	ds_read_b128 v[18:21], v98 offset:400
	ds_read_b128 v[22:25], v38 offset:61392
	ds_read_b128 v[26:29], v98 offset:464
	s_waitcnt lgkmcnt(2)
	v_mfma_f32_16x16x32_f16 v[6:9], v[14:17], v[18:21], v[6:9]
	ds_read_b128 v[18:21], v111 offset:400
	ds_read_b128 v[30:33], v111 offset:464
	s_waitcnt lgkmcnt(1)
	v_mfma_f32_16x16x32_f16 v[10:13], v[14:17], v[18:21], v[10:13]
	ds_read_b128 v[18:21], v117 offset:400
	ds_read_b128 v[34:37], v117 offset:464
	s_waitcnt lgkmcnt(1)
	v_mfma_f32_16x16x32_f16 v[2:5], v[14:17], v[18:21], v[2:5]
	v_mad_u32_u24 v14, v46, 10, v85
	v_mad_u32_u24 v38, v14, s0, v84
	ds_read_b128 v[14:17], v38 offset:61200
	v_mfma_f32_16x16x32_f16 v[6:9], v[22:25], v[26:29], v[6:9]
	v_mfma_f32_16x16x32_f16 v[10:13], v[22:25], v[30:33], v[10:13]
	s_waitcnt lgkmcnt(1)
	v_mfma_f32_16x16x32_f16 v[2:5], v[22:25], v[34:37], v[2:5]
	ds_read_b128 v[18:21], v98 offset:544
	ds_read_b128 v[22:25], v38 offset:61264
	ds_read_b128 v[26:29], v98 offset:608
	s_waitcnt lgkmcnt(2)
	v_mfma_f32_16x16x32_f16 v[6:9], v[14:17], v[18:21], v[6:9]
	ds_read_b128 v[18:21], v111 offset:544
	ds_read_b128 v[30:33], v111 offset:608
	s_waitcnt lgkmcnt(1)
	v_mfma_f32_16x16x32_f16 v[10:13], v[14:17], v[18:21], v[10:13]
	ds_read_b128 v[18:21], v117 offset:544
	ds_read_b128 v[34:37], v117 offset:608
	s_waitcnt lgkmcnt(1)
	v_mfma_f32_16x16x32_f16 v[2:5], v[14:17], v[18:21], v[2:5]
	ds_read_b128 v[14:17], v38 offset:61328
	v_mfma_f32_16x16x32_f16 v[6:9], v[22:25], v[26:29], v[6:9]
	v_mfma_f32_16x16x32_f16 v[10:13], v[22:25], v[30:33], v[10:13]
	s_waitcnt lgkmcnt(1)
	v_mfma_f32_16x16x32_f16 v[2:5], v[22:25], v[34:37], v[2:5]
	ds_read_b128 v[18:21], v98 offset:672
	ds_read_b128 v[22:25], v38 offset:61392
	ds_read_b128 v[26:29], v98 offset:736
	v_mad_u32_u24 v38, v46, 10, 10
	s_waitcnt lgkmcnt(2)
	v_mfma_f32_16x16x32_f16 v[6:9], v[14:17], v[18:21], v[6:9]
	ds_read_b128 v[18:21], v111 offset:672
	ds_read_b128 v[30:33], v111 offset:736
	s_waitcnt lgkmcnt(1)
	v_mfma_f32_16x16x32_f16 v[10:13], v[14:17], v[18:21], v[10:13]
	ds_read_b128 v[18:21], v117 offset:672
	ds_read_b128 v[34:37], v117 offset:736
	s_waitcnt lgkmcnt(1)
	v_mfma_f32_16x16x32_f16 v[2:5], v[14:17], v[18:21], v[2:5]
	v_add_u32_e32 v14, v47, v38
	v_mad_u32_u24 v39, v14, s0, v84
	ds_read_b128 v[14:17], v39 offset:61200
	v_mfma_f32_16x16x32_f16 v[6:9], v[22:25], v[26:29], v[6:9]
	v_mfma_f32_16x16x32_f16 v[10:13], v[22:25], v[30:33], v[10:13]
	s_waitcnt lgkmcnt(1)
	v_mfma_f32_16x16x32_f16 v[2:5], v[22:25], v[34:37], v[2:5]
	ds_read_b128 v[18:21], v98 offset:4080
	ds_read_b128 v[22:25], v39 offset:61264
	ds_read_b128 v[26:29], v98 offset:4144
	s_waitcnt lgkmcnt(2)
	v_mfma_f32_16x16x32_f16 v[6:9], v[14:17], v[18:21], v[6:9]
	ds_read_b128 v[18:21], v111 offset:4080
	ds_read_b128 v[30:33], v111 offset:4144
	s_waitcnt lgkmcnt(1)
	v_mfma_f32_16x16x32_f16 v[10:13], v[14:17], v[18:21], v[10:13]
	ds_read_b128 v[18:21], v117 offset:4080
	ds_read_b128 v[34:37], v117 offset:4144
	s_waitcnt lgkmcnt(1)
	v_mfma_f32_16x16x32_f16 v[2:5], v[14:17], v[18:21], v[2:5]
	ds_read_b128 v[14:17], v39 offset:61328
	v_mfma_f32_16x16x32_f16 v[6:9], v[22:25], v[26:29], v[6:9]
	v_mfma_f32_16x16x32_f16 v[10:13], v[22:25], v[30:33], v[10:13]
	s_waitcnt lgkmcnt(1)
	v_mfma_f32_16x16x32_f16 v[2:5], v[22:25], v[34:37], v[2:5]
	ds_read_b128 v[18:21], v98 offset:4208
	ds_read_b128 v[22:25], v39 offset:61392
	ds_read_b128 v[26:29], v98 offset:4272
	s_waitcnt lgkmcnt(2)
	v_mfma_f32_16x16x32_f16 v[6:9], v[14:17], v[18:21], v[6:9]
	ds_read_b128 v[18:21], v111 offset:4208
	ds_read_b128 v[30:33], v111 offset:4272
	s_waitcnt lgkmcnt(1)
	v_mfma_f32_16x16x32_f16 v[10:13], v[14:17], v[18:21], v[10:13]
	ds_read_b128 v[18:21], v117 offset:4208
	ds_read_b128 v[34:37], v117 offset:4272
	s_waitcnt lgkmcnt(1)
	v_mfma_f32_16x16x32_f16 v[2:5], v[14:17], v[18:21], v[2:5]
	v_add_u32_e32 v14, v58, v38
	v_mad_u32_u24 v39, v14, s0, v84
	ds_read_b128 v[14:17], v39 offset:61200
	v_mfma_f32_16x16x32_f16 v[6:9], v[22:25], v[26:29], v[6:9]
	v_mfma_f32_16x16x32_f16 v[10:13], v[22:25], v[30:33], v[10:13]
	s_waitcnt lgkmcnt(1)
	v_mfma_f32_16x16x32_f16 v[2:5], v[22:25], v[34:37], v[2:5]
	ds_read_b128 v[18:21], v98 offset:4352
	ds_read_b128 v[22:25], v39 offset:61264
	ds_read_b128 v[26:29], v98 offset:4416
	s_waitcnt lgkmcnt(2)
	v_mfma_f32_16x16x32_f16 v[6:9], v[14:17], v[18:21], v[6:9]
	ds_read_b128 v[18:21], v111 offset:4352
	ds_read_b128 v[30:33], v111 offset:4416
	s_waitcnt lgkmcnt(1)
	v_mfma_f32_16x16x32_f16 v[10:13], v[14:17], v[18:21], v[10:13]
	ds_read_b128 v[18:21], v117 offset:4352
	ds_read_b128 v[34:37], v117 offset:4416
	s_waitcnt lgkmcnt(1)
	v_mfma_f32_16x16x32_f16 v[2:5], v[14:17], v[18:21], v[2:5]
	ds_read_b128 v[14:17], v39 offset:61328
	v_mfma_f32_16x16x32_f16 v[6:9], v[22:25], v[26:29], v[6:9]
	v_mfma_f32_16x16x32_f16 v[10:13], v[22:25], v[30:33], v[10:13]
	s_waitcnt lgkmcnt(1)
	v_mfma_f32_16x16x32_f16 v[2:5], v[22:25], v[34:37], v[2:5]
	ds_read_b128 v[18:21], v98 offset:4480
	ds_read_b128 v[22:25], v39 offset:61392
	ds_read_b128 v[26:29], v98 offset:4544
	s_waitcnt lgkmcnt(2)
	v_mfma_f32_16x16x32_f16 v[6:9], v[14:17], v[18:21], v[6:9]
	ds_read_b128 v[18:21], v111 offset:4480
	ds_read_b128 v[30:33], v111 offset:4544
	s_waitcnt lgkmcnt(1)
	v_mfma_f32_16x16x32_f16 v[10:13], v[14:17], v[18:21], v[10:13]
	ds_read_b128 v[18:21], v117 offset:4480
	ds_read_b128 v[34:37], v117 offset:4544
	s_waitcnt lgkmcnt(1)
	v_mfma_f32_16x16x32_f16 v[2:5], v[14:17], v[18:21], v[2:5]
	v_add_u32_e32 v14, v85, v38
	v_mad_u32_u24 v38, v14, s0, v84
	ds_read_b128 v[14:17], v38 offset:61200
	v_mfma_f32_16x16x32_f16 v[6:9], v[22:25], v[26:29], v[6:9]
	v_mfma_f32_16x16x32_f16 v[10:13], v[22:25], v[30:33], v[10:13]
	s_waitcnt lgkmcnt(1)
	v_mfma_f32_16x16x32_f16 v[2:5], v[22:25], v[34:37], v[2:5]
	ds_read_b128 v[18:21], v98 offset:4624
	ds_read_b128 v[22:25], v38 offset:61264
	ds_read_b128 v[26:29], v98 offset:4688
	s_waitcnt lgkmcnt(2)
	v_mfma_f32_16x16x32_f16 v[6:9], v[14:17], v[18:21], v[6:9]
	ds_read_b128 v[18:21], v111 offset:4624
	ds_read_b128 v[30:33], v111 offset:4688
	s_waitcnt lgkmcnt(1)
	v_mfma_f32_16x16x32_f16 v[10:13], v[14:17], v[18:21], v[10:13]
	ds_read_b128 v[18:21], v117 offset:4624
	ds_read_b128 v[34:37], v117 offset:4688
	s_waitcnt lgkmcnt(1)
	v_mfma_f32_16x16x32_f16 v[2:5], v[14:17], v[18:21], v[2:5]
	ds_read_b128 v[14:17], v38 offset:61328
	ds_read_b128 v[18:21], v98 offset:4752
	v_mfma_f32_16x16x32_f16 v[6:9], v[22:25], v[26:29], v[6:9]
	v_mfma_f32_16x16x32_f16 v[10:13], v[22:25], v[30:33], v[10:13]
	s_waitcnt lgkmcnt(2)
	v_mfma_f32_16x16x32_f16 v[22:25], v[22:25], v[34:37], v[2:5]
	s_nop 2
	ds_read_b128 v[2:5], v111 offset:4752
	ds_read_b128 v[26:29], v38 offset:61392
	ds_read_b128 v[30:33], v98 offset:4816
	ds_read_b128 v[34:37], v117 offset:4752
	ds_read_b128 v[38:41], v111 offset:4816
	s_waitcnt lgkmcnt(5)
	v_mfma_f32_16x16x32_f16 v[18:21], v[14:17], v[18:21], v[6:9]
	s_waitcnt lgkmcnt(4)
	v_mfma_f32_16x16x32_f16 v[10:13], v[14:17], v[2:5], v[10:13]
	s_nop 0
	global_load_dwordx4 v[6:9], v[70:71], off nt
	global_load_dwordx4 v[2:5], v[42:43], off nt
	ds_read_b128 v[42:45], v117 offset:4816
	s_waitcnt lgkmcnt(2)
	v_mfma_f32_16x16x32_f16 v[14:17], v[14:17], v[34:37], v[22:25]
	s_nop 2
	v_add_u32_e32 v22, v47, v90
	v_mad_u32_u24 v56, v22, s0, v84
	ds_read_b128 v[22:25], v56 offset:61200
	v_mfma_f32_16x16x32_f16 v[18:21], v[26:29], v[30:33], v[18:21]
	ds_read_b128 v[30:33], v98 offset:8160
	s_waitcnt lgkmcnt(3)
	v_mfma_f32_16x16x32_f16 v[10:13], v[26:29], v[38:41], v[10:13]
	s_waitcnt lgkmcnt(2)
	v_mfma_f32_16x16x32_f16 v[14:17], v[26:29], v[42:45], v[14:17]
	ds_read_b128 v[26:29], v111 offset:8160
	ds_read_b128 v[34:37], v56 offset:61264
	ds_read_b128 v[38:41], v98 offset:8224
	s_waitcnt lgkmcnt(3)
	v_mfma_f32_16x16x32_f16 v[18:21], v[22:25], v[30:33], v[18:21]
	ds_read_b128 v[30:33], v117 offset:8160
	ds_read_b128 v[42:45], v111 offset:8224
	ds_read_b128 v[46:49], v117 offset:8224
	s_waitcnt lgkmcnt(5)
	v_mfma_f32_16x16x32_f16 v[26:29], v[22:25], v[26:29], v[10:13]
	s_waitcnt lgkmcnt(2)
	v_mfma_f32_16x16x32_f16 v[22:25], v[22:25], v[30:33], v[14:17]
	s_nop 2
	global_load_dwordx4 v[14:17], v[50:51], off nt
	global_load_dwordx4 v[10:13], v[52:53], off nt
	ds_read_b128 v[30:33], v56 offset:61328
	v_mfma_f32_16x16x32_f16 v[18:21], v[34:37], v[38:41], v[18:21]
	ds_read_b128 v[38:41], v98 offset:8288
	s_waitcnt lgkmcnt(3)
	v_mfma_f32_16x16x32_f16 v[26:29], v[34:37], v[42:45], v[26:29]
	s_waitcnt lgkmcnt(2)
	v_mfma_f32_16x16x32_f16 v[22:25], v[34:37], v[46:49], v[22:25]
	ds_read_b128 v[34:37], v111 offset:8288
	ds_read_b128 v[42:45], v56 offset:61392
	ds_read_b128 v[46:49], v98 offset:8352
	v_add_co_u32_e32 v56, vcc, 0xa00000, v70
	s_waitcnt lgkmcnt(3)
	v_mfma_f32_16x16x32_f16 v[38:41], v[30:33], v[38:41], v[18:21]
	s_nop 2
	ds_read_b128 v[18:21], v117 offset:8288
	ds_read_b128 v[50:53], v111 offset:8352
	v_addc_co_u32_e32 v57, vcc, 0, v71, vcc
	s_waitcnt lgkmcnt(2)
	v_mfma_f32_16x16x32_f16 v[38:41], v[42:45], v[46:49], v[38:41]
	v_add_u32_e32 v46, v58, v90
	v_mad_u32_u24 v80, v46, s0, v84
	v_add_co_u32_e32 v76, vcc, 0xc00000, v70
	v_mfma_f32_16x16x32_f16 v[26:29], v[30:33], v[34:37], v[26:29]
	ds_read_b128 v[34:37], v117 offset:8352
	v_addc_co_u32_e32 v77, vcc, 0, v71, vcc
	s_waitcnt lgkmcnt(2)
	v_mfma_f32_16x16x32_f16 v[30:33], v[30:33], v[18:21], v[22:25]
	s_nop 2
	global_load_dwordx4 v[22:25], v[54:55], off nt
	global_load_dwordx4 v[18:21], v[56:57], off nt
	ds_read_b128 v[46:49], v80 offset:61200
	v_add_co_u32_e32 v78, vcc, 0xe00000, v70
	s_waitcnt lgkmcnt(2)
	v_mfma_f32_16x16x32_f16 v[26:29], v[42:45], v[50:53], v[26:29]
	ds_read_b128 v[50:53], v98 offset:8432
	v_addc_co_u32_e32 v79, vcc, 0, v71, vcc
	s_waitcnt lgkmcnt(2)
	v_mfma_f32_16x16x32_f16 v[30:33], v[42:45], v[34:37], v[30:33]
	ds_read_b128 v[34:37], v111 offset:8432
	ds_read_b128 v[42:45], v80 offset:61264
	ds_read_b128 v[54:57], v98 offset:8496
	v_add_co_u32_e32 v74, vcc, s1, v82
	s_waitcnt lgkmcnt(3)
	v_mfma_f32_16x16x32_f16 v[38:41], v[46:49], v[50:53], v[38:41]
	ds_read_b128 v[50:53], v117 offset:8432
	ds_read_b128 v[58:61], v111 offset:8496
	ds_read_b128 v[70:73], v117 offset:8496
	v_addc_co_u32_e32 v75, vcc, 0, v83, vcc
	s_waitcnt lgkmcnt(5)
	v_mfma_f32_16x16x32_f16 v[66:69], v[46:49], v[34:37], v[26:29]
	global_load_dwordx4 v[34:37], v[76:77], off nt
	s_nop 1
	global_load_dwordx4 v[26:29], v[78:79], off nt
	v_add_co_u32_e32 v88, vcc, s2, v82
	s_waitcnt lgkmcnt(2)
	v_mfma_f32_16x16x32_f16 v[30:33], v[46:49], v[50:53], v[30:33]
	ds_read_b128 v[46:49], v80 offset:61328
	v_addc_co_u32_e32 v89, vcc, 0, v83, vcc
	v_mfma_f32_16x16x32_f16 v[38:41], v[42:45], v[54:57], v[38:41]
	ds_read_b128 v[54:57], v98 offset:8560
	s_movk_i32 s2, 0xa9
	s_waitcnt lgkmcnt(3)
	v_mfma_f32_16x16x32_f16 v[50:53], v[42:45], v[58:61], v[66:69]
	s_waitcnt lgkmcnt(2)
	v_mfma_f32_16x16x32_f16 v[42:45], v[42:45], v[70:73], v[30:33]
	ds_read_b128 v[58:61], v111 offset:8560
	ds_read_b128 v[66:69], v80 offset:61392
	ds_read_b128 v[70:73], v98 offset:8624
	s_waitcnt lgkmcnt(3)
	v_mfma_f32_16x16x32_f16 v[54:57], v[46:49], v[54:57], v[38:41]
	s_nop 2
	global_load_dwordx4 v[38:41], v[82:83], off nt
	global_load_dwordx4 v[30:33], v[74:75], off nt
	ds_read_b128 v[74:77], v117 offset:8560
	ds_read_b128 v[78:81], v111 offset:8624
	s_waitcnt lgkmcnt(4)
	v_mfma_f32_16x16x32_f16 v[50:53], v[46:49], v[58:61], v[50:53]
	ds_read_b128 v[58:61], v117 offset:8624
	s_waitcnt lgkmcnt(2)
	v_mfma_f32_16x16x32_f16 v[42:45], v[46:49], v[74:77], v[42:45]
	v_mfma_f32_16x16x32_f16 v[46:49], v[66:69], v[70:73], v[54:57]
	ds_read_b128 v[70:73], v98 offset:8704
	s_nop 1
	v_add_u32_e32 v54, v85, v90
	v_mad_u32_u24 v92, v54, s0, v84
	ds_read_b128 v[54:57], v92 offset:61200
	s_waitcnt lgkmcnt(3)
	v_mfma_f32_16x16x32_f16 v[50:53], v[66:69], v[78:81], v[50:53]
	v_add_co_u32_e32 v90, vcc, s3, v82
	s_add_i32 s0, 0, 0x13550
	s_waitcnt lgkmcnt(2)
	v_mfma_f32_16x16x32_f16 v[58:61], v[66:69], v[58:61], v[42:45]
	s_nop 2
	ds_read_b128 v[42:45], v111 offset:8704
	ds_read_b128 v[66:69], v92 offset:61264
	ds_read_b128 v[74:77], v98 offset:8768
	v_addc_co_u32_e32 v91, vcc, 0, v83, vcc
	s_waitcnt lgkmcnt(3)
	v_mfma_f32_16x16x32_f16 v[70:73], v[54:57], v[70:73], v[46:49]
	ds_read_b128 v[78:81], v117 offset:8704
	ds_read_b128 v[82:85], v111 offset:8768
	v_cmp_gt_u32_e64 s[2:3], s2, v64
	v_cmp_eq_u32_e32 vcc, 0, v97
	s_waitcnt lgkmcnt(4)
	v_mfma_f32_16x16x32_f16 v[50:53], v[54:57], v[42:45], v[50:53]
	global_load_dwordx4 v[46:49], v[88:89], off nt
	global_load_dwordx4 v[42:45], v[90:91], off nt
	ds_read_b128 v[88:91], v117 offset:8768
	s_waitcnt lgkmcnt(2)
	v_mfma_f32_16x16x32_f16 v[54:57], v[54:57], v[78:81], v[58:61]
	s_nop 2
	ds_read_b128 v[58:61], v92 offset:61328
	ds_read_b128 v[92:95], v92 offset:61392
	ds_read_b128 v[78:81], v98 offset:8832
	ds_read_b128 v[98:101], v98 offset:8896
	ds_read_b128 v[106:109], v111 offset:8832
	ds_read_b128 v[118:121], v111 offset:8896
	ds_read_b128 v[122:125], v117 offset:8832
	ds_read_b128 v[126:129], v117 offset:8896
	v_mfma_f32_16x16x32_f16 v[102:105], v[66:69], v[74:77], v[70:73]
	s_waitcnt lgkmcnt(9)
	v_mfma_f32_16x16x32_f16 v[50:53], v[66:69], v[82:85], v[50:53]
	s_nop 0
	v_lshlrev_b32_e32 v70, 2, v62
	v_lshl_or_b32 v73, v65, 4, v70
	v_lshl_add_u32 v75, v73, 2, 0
	s_waitcnt lgkmcnt(8)
	v_mfma_f32_16x16x32_f16 v[66:69], v[66:69], v[88:91], v[54:57]
	v_add_u32_e32 v65, 0x13810, v75
	v_min_u32_e32 v72, 0xaf, v64
	v_lshl_add_u32 v70, v63, 2, s0
	s_waitcnt lgkmcnt(5)
	v_mfma_f32_16x16x32_f16 v[54:57], v[58:61], v[78:81], v[102:105]
	v_lshl_add_u32 v71, v110, 2, s0
	v_lshl_add_u32 v72, v72, 2, s0
	ds_read_b32 v65, v65
	ds_read_b32 v79, v70
	ds_read_b32 v78, v71
	ds_read_b32 v77, v72
	s_waitcnt lgkmcnt(7)
	v_mfma_f32_16x16x32_f16 v[80:83], v[58:61], v[106:109], v[50:53]
	s_movk_i32 s0, 0x69
	v_cmp_gt_u32_e64 s[0:1], s0, v63
	s_waitcnt lgkmcnt(5)
	v_mfma_f32_16x16x32_f16 v[58:61], v[58:61], v[122:125], v[66:69]
	v_mfma_f32_16x16x32_f16 v[50:53], v[92:95], v[98:101], v[54:57]
	v_mfma_f32_16x16x32_f16 v[54:57], v[92:95], v[118:121], v[80:83]
	s_waitcnt lgkmcnt(4)
	v_mfma_f32_16x16x32_f16 v[58:61], v[92:95], v[126:129], v[58:61]
	s_waitcnt lgkmcnt(2)
	s_nop 3
	v_or_b32_e32 v69, 1, v73
	v_or_b32_e32 v64, 2, v73
	v_or_b32_e32 v152, 3, v73
	v_lshl_add_u32 v71, v69, 2, 0
	v_lshl_add_u32 v66, v64, 2, 0
	v_lshl_add_u32 v153, v152, 2, 0
	v_add_u32_e32 v160, 0x13810, v71
	v_add_u32_e32 v161, 0x13810, v66
	v_add_u32_e32 v162, 0x13810, v153
	ds_read_b32 v160, v160
	ds_read_b32 v161, v161
	ds_read_b32 v162, v162
	v_mov_b32_e32 v155, 0xff800000
	s_waitcnt lgkmcnt(3)
	v_mul_f32_e32 v164, v50, v79
	v_mul_f32_e32 v165, v54, v78
	v_mul_f32_e32 v166, v58, v77
	v_mul_f32_e32 v164, v65, v164
	v_mul_f32_e32 v165, v65, v165
	v_mul_f32_e32 v166, v65, v166
	v_mul_f32_e32 v167, v51, v79
	v_mul_f32_e32 v168, v55, v78
	v_mul_f32_e32 v169, v59, v77
	v_mul_f32_e32 v170, v52, v79
	v_mul_f32_e32 v171, v56, v78
	v_mul_f32_e32 v172, v60, v77
	v_mul_f32_e32 v173, v53, v79
	v_mul_f32_e32 v174, v57, v78
	v_mul_f32_e32 v175, v61, v77
	s_waitcnt lgkmcnt(0)
	v_mul_f32_e32 v167, v160, v167
	v_mul_f32_e32 v168, v160, v168
	v_mul_f32_e32 v169, v160, v169
	v_mul_f32_e32 v170, v161, v170
	v_mul_f32_e32 v171, v161, v171
	v_mul_f32_e32 v172, v161, v172
	v_mul_f32_e32 v173, v162, v173
	v_mul_f32_e32 v174, v162, v174
	v_mul_f32_e32 v175, v162, v175
	v_cndmask_b32_e64 v165, v155, v165, s[0:1]
	v_cndmask_b32_e64 v166, v155, v166, s[2:3]
	v_cndmask_b32_e64 v168, v155, v168, s[0:1]
	v_cndmask_b32_e64 v169, v155, v169, s[2:3]
	v_cndmask_b32_e64 v171, v155, v171, s[0:1]
	v_cndmask_b32_e64 v172, v155, v172, s[2:3]
	v_cndmask_b32_e64 v174, v155, v174, s[0:1]
	v_cndmask_b32_e64 v175, v155, v175, s[2:3]
	v_max_f32_e32 v176, 0xff800000, v164
	v_max_f32_e32 v177, 0xff800000, v167
	v_max_f32_e32 v178, 0xff800000, v170
	v_max_f32_e32 v179, 0xff800000, v173
	v_max3_f32 v176, v176, v165, v166
	v_max3_f32 v177, v177, v168, v169
	v_max3_f32 v178, v178, v171, v172
	v_max3_f32 v179, v179, v174, v175
	v_max_f32_dpp v176, v176, v176 quad_perm:[1,0,3,2] row_mask:0xf bank_mask:0xf
	v_max_f32_dpp v177, v177, v177 quad_perm:[1,0,3,2] row_mask:0xf bank_mask:0xf
	v_max_f32_dpp v178, v178, v178 quad_perm:[1,0,3,2] row_mask:0xf bank_mask:0xf
	v_max_f32_dpp v179, v179, v179 quad_perm:[1,0,3,2] row_mask:0xf bank_mask:0xf
	v_max_f32_dpp v176, v176, v176 quad_perm:[2,3,0,1] row_mask:0xf bank_mask:0xf
	v_max_f32_dpp v177, v177, v177 quad_perm:[2,3,0,1] row_mask:0xf bank_mask:0xf
	v_max_f32_dpp v178, v178, v178 quad_perm:[2,3,0,1] row_mask:0xf bank_mask:0xf
	v_max_f32_dpp v179, v179, v179 quad_perm:[2,3,0,1] row_mask:0xf bank_mask:0xf
	v_max_f32_dpp v176, v176, v176 row_half_mirror row_mask:0xf bank_mask:0xf
	v_max_f32_dpp v177, v177, v177 row_half_mirror row_mask:0xf bank_mask:0xf
	v_max_f32_dpp v178, v178, v178 row_half_mirror row_mask:0xf bank_mask:0xf
	v_max_f32_dpp v179, v179, v179 row_half_mirror row_mask:0xf bank_mask:0xf
	v_max_f32_dpp v176, v176, v176 row_mirror row_mask:0xf bank_mask:0xf
	v_max_f32_dpp v177, v177, v177 row_mirror row_mask:0xf bank_mask:0xf
	v_max_f32_dpp v178, v178, v178 row_mirror row_mask:0xf bank_mask:0xf
	v_max_f32_dpp v179, v179, v179 row_mirror row_mask:0xf bank_mask:0xf
	v_and_b32_e32 v58, 0x180, v0
	v_add_u32_e32 v58, s6, v58
	v_lshl_add_u32 v58, v73, 2, v58
	s_and_saveexec_b64 s[6:7], vcc
	ds_write_b128 v58, v[176:179]
	s_or_b64 exec, exec, s[6:7]
	v_mov_b32_e32 v76, v164
	v_mov_b32_e32 v74, v165
	v_mov_b32_e32 v72, v166
	v_mov_b32_e32 v70, v167
	v_mov_b32_e32 v68, v168
	v_mov_b32_e32 v67, v169
	v_mov_b32_e32 v65, v170
	v_mov_b32_e32 v59, v171
	v_mov_b32_e32 v56, v172
	v_mov_b32_e32 v53, v173
	v_mov_b32_e32 v52, v174
	v_mov_b32_e32 v50, v175
	v_mov_b32_e32 v54, v152
	v_mov_b32_e32 v55, v153
	v_add_u32_e32 v51, 0x13890, v75
	s_waitcnt lgkmcnt(0)
	s_barrier
	v_add_u32_e32 v152, 0x13890, v75
	ds_read_b128 v[156:159], v152
	ds_read_b128 v[160:163], v152 offset:128
	ds_read_b128 v[164:167], v152 offset:256
	ds_read_b128 v[168:171], v152 offset:384
	v_lshlrev_b32_e32 v51, 3, v62
	v_lshlrev_b32_e32 v60, 8, v73
	v_or_b32_e32 v172, v63, v60
	s_waitcnt lgkmcnt(0)
	v_max_f32_e32 v173, v156, v160
	v_max_f32_e32 v174, v157, v161
	v_max_f32_e32 v175, v158, v162
	v_max_f32_e32 v176, v159, v163
	v_max3_f32 v173, v173, v164, v168
	v_max3_f32 v174, v174, v165, v169
	v_max3_f32 v175, v175, v166, v170
	v_max3_f32 v176, v176, v167, v171
	v_add_f32_e32 v173, 0xbb102de0, v173
	v_add_f32_e32 v174, 0xbb102de0, v174
	v_add_f32_e32 v175, 0xbb102de0, v175
	v_add_f32_e32 v176, 0xbb102de0, v176
	v_cmp_ge_f32_e64 s[90:91], v76, v173
	v_cmp_ge_f32_e64 s[92:93], v74, v173
	v_cmp_ge_f32_e64 s[94:95], v72, v173
	v_cmp_ge_f32_e64 s[96:97], v70, v174
	v_cmp_ge_f32_e64 s[98:99], v68, v174
	v_cmp_ge_f32_e64 s[60:61], v67, v174
	v_cmp_ge_f32_e64 s[62:63], v65, v175
	v_cmp_ge_f32_e64 s[88:89], v59, v175
	v_cmp_ge_f32_e64 s[6:7], v56, v175
	v_cmp_ge_f32_e64 s[8:9], v53, v176
	v_cmp_ge_f32_e64 s[2:3], v52, v176
	v_cmp_ge_f32_e64 s[80:81], v50, v176
	s_bcnt1_i32_b64 s13, s[90:91]
	s_bcnt1_i32_b64 s1, s[92:93]
	s_add_u32 s13, s13, s1
	s_bcnt1_i32_b64 s1, s[94:95]
	s_add_u32 s13, s13, s1
	s_bcnt1_i32_b64 s1, s[96:97]
	s_add_u32 s13, s13, s1
	s_bcnt1_i32_b64 s1, s[98:99]
	s_add_u32 s13, s13, s1
	s_bcnt1_i32_b64 s1, s[60:61]
	s_add_u32 s13, s13, s1
	s_bcnt1_i32_b64 s1, s[62:63]
	s_add_u32 s13, s13, s1
	s_bcnt1_i32_b64 s1, s[88:89]
	s_add_u32 s13, s13, s1
	s_bcnt1_i32_b64 s1, s[6:7]
	s_add_u32 s13, s13, s1
	s_bcnt1_i32_b64 s1, s[8:9]
	s_add_u32 s13, s13, s1
	s_bcnt1_i32_b64 s1, s[2:3]
	s_add_u32 s13, s13, s1
	s_bcnt1_i32_b64 s1, s[80:81]
	s_add_u32 s13, s13, s1
	s_cmp_eq_u32 s13, 0
	s_cbranch_scc1 .Lmy_list_done
	v_mov_b32_e32 v177, 0x13d90
	v_mov_b32_e32 v178, s13
	s_mov_b64 exec, 1
	ds_add_rtn_u32 v179, v177, v178
	s_mov_b64 exec, -1
	s_waitcnt lgkmcnt(0)
	v_readfirstlane_b32 s0, v179
	s_and_saveexec_b64 s[82:83], s[90:91]
	s_cbranch_execz .Lmy_list_skip0
	v_mbcnt_lo_u32_b32 v180, s90, 0
	v_mbcnt_hi_u32_b32 v180, s91, v180
	v_add_u32_e32 v181, 0x0, v172
	v_add_lshl_u32 v180, v180, s0, 1
	ds_write_b16 v180, v181
	s_bcnt1_i32_b64 s1, s[90:91]
	s_add_u32 s0, s0, s1
.Lmy_list_skip0:
	s_or_b64 exec, exec, s[82:83]
	s_and_saveexec_b64 s[82:83], s[92:93]
	s_cbranch_execz .Lmy_list_skip1
	v_mbcnt_lo_u32_b32 v180, s92, 0
	v_mbcnt_hi_u32_b32 v180, s93, v180
	v_add_u32_e32 v181, 0x40, v172
	v_add_lshl_u32 v180, v180, s0, 1
	ds_write_b16 v180, v181
	s_bcnt1_i32_b64 s1, s[92:93]
	s_add_u32 s0, s0, s1
.Lmy_list_skip1:
	s_or_b64 exec, exec, s[82:83]
	s_and_saveexec_b64 s[82:83], s[94:95]
	s_cbranch_execz .Lmy_list_skip2
	v_mbcnt_lo_u32_b32 v180, s94, 0
	v_mbcnt_hi_u32_b32 v180, s95, v180
	v_add_u32_e32 v181, 0x80, v172
	v_add_lshl_u32 v180, v180, s0, 1
	ds_write_b16 v180, v181
	s_bcnt1_i32_b64 s1, s[94:95]
	s_add_u32 s0, s0, s1
.Lmy_list_skip2:
	s_or_b64 exec, exec, s[82:83]
	s_and_saveexec_b64 s[82:83], s[96:97]
	s_cbranch_execz .Lmy_list_skip3
	v_mbcnt_lo_u32_b32 v180, s96, 0
	v_mbcnt_hi_u32_b32 v180, s97, v180
	v_add_u32_e32 v181, 0x100, v172
	v_add_lshl_u32 v180, v180, s0, 1
	ds_write_b16 v180, v181
	s_bcnt1_i32_b64 s1, s[96:97]
	s_add_u32 s0, s0, s1
.Lmy_list_skip3:
	s_or_b64 exec, exec, s[82:83]
	s_and_saveexec_b64 s[82:83], s[98:99]
	s_cbranch_execz .Lmy_list_skip4
	v_mbcnt_lo_u32_b32 v180, s98, 0
	v_mbcnt_hi_u32_b32 v180, s99, v180
	v_add_u32_e32 v181, 0x140, v172
	v_add_lshl_u32 v180, v180, s0, 1
	ds_write_b16 v180, v181
	s_bcnt1_i32_b64 s1, s[98:99]
	s_add_u32 s0, s0, s1
.Lmy_list_skip4:
	s_or_b64 exec, exec, s[82:83]
	s_and_saveexec_b64 s[82:83], s[60:61]
	s_cbranch_execz .Lmy_list_skip5
	v_mbcnt_lo_u32_b32 v180, s60, 0
	v_mbcnt_hi_u32_b32 v180, s61, v180
	v_add_u32_e32 v181, 0x180, v172
	v_add_lshl_u32 v180, v180, s0, 1
	ds_write_b16 v180, v181
	s_bcnt1_i32_b64 s1, s[60:61]
	s_add_u32 s0, s0, s1
.Lmy_list_skip5:
	s_or_b64 exec, exec, s[82:83]
	s_and_saveexec_b64 s[82:83], s[62:63]
	s_cbranch_execz .Lmy_list_skip6
	v_mbcnt_lo_u32_b32 v180, s62, 0
	v_mbcnt_hi_u32_b32 v180, s63, v180
	v_add_u32_e32 v181, 0x200, v172
	v_add_lshl_u32 v180, v180, s0, 1
	ds_write_b16 v180, v181
	s_bcnt1_i32_b64 s1, s[62:63]
	s_add_u32 s0, s0, s1
.Lmy_list_skip6:
	s_or_b64 exec, exec, s[82:83]
	s_and_saveexec_b64 s[82:83], s[88:89]
	s_cbranch_execz .Lmy_list_skip7
	v_mbcnt_lo_u32_b32 v180, s88, 0
	v_mbcnt_hi_u32_b32 v180, s89, v180
	v_add_u32_e32 v181, 0x240, v172
	v_add_lshl_u32 v180, v180, s0, 1
	ds_write_b16 v180, v181
	s_bcnt1_i32_b64 s1, s[88:89]
	s_add_u32 s0, s0, s1
.Lmy_list_skip7:
	s_or_b64 exec, exec, s[82:83]
	s_and_saveexec_b64 s[82:83], s[6:7]
	s_cbranch_execz .Lmy_list_skip8
	v_mbcnt_lo_u32_b32 v180, s6, 0
	v_mbcnt_hi_u32_b32 v180, s7, v180
	v_add_u32_e32 v181, 0x280, v172
	v_add_lshl_u32 v180, v180, s0, 1
	ds_write_b16 v180, v181
	s_bcnt1_i32_b64 s1, s[6:7]
	s_add_u32 s0, s0, s1
.Lmy_list_skip8:
	s_or_b64 exec, exec, s[82:83]
	s_and_saveexec_b64 s[82:83], s[8:9]
	s_cbranch_execz .Lmy_list_skip9
	v_mbcnt_lo_u32_b32 v180, s8, 0
	v_mbcnt_hi_u32_b32 v180, s9, v180
	v_add_u32_e32 v181, 0x300, v172
	v_add_lshl_u32 v180, v180, s0, 1
	ds_write_b16 v180, v181
	s_bcnt1_i32_b64 s1, s[8:9]
	s_add_u32 s0, s0, s1
.Lmy_list_skip9:
	s_or_b64 exec, exec, s[82:83]
	s_and_saveexec_b64 s[82:83], s[2:3]
	s_cbranch_execz .Lmy_list_skip10
	v_mbcnt_lo_u32_b32 v180, s2, 0
	v_mbcnt_hi_u32_b32 v180, s3, v180
	v_add_u32_e32 v181, 0x340, v172
	v_add_lshl_u32 v180, v180, s0, 1
	ds_write_b16 v180, v181
	s_bcnt1_i32_b64 s1, s[2:3]
	s_add_u32 s0, s0, s1
.Lmy_list_skip10:
	s_or_b64 exec, exec, s[82:83]
	s_and_saveexec_b64 s[82:83], s[80:81]
	s_cbranch_execz .Lmy_list_skip11
	v_mbcnt_lo_u32_b32 v180, s80, 0
	v_mbcnt_hi_u32_b32 v180, s81, v180
	v_add_u32_e32 v181, 0x380, v172
	v_add_lshl_u32 v180, v180, s0, 1
	ds_write_b16 v180, v181
	s_bcnt1_i32_b64 s1, s[80:81]
	s_add_u32 s0, s0, s1
.Lmy_list_skip11:
	s_or_b64 exec, exec, s[82:83]
.Lmy_list_done:
	s_add_i32 s0, 0, 0x13d90
	v_mov_b32_e32 v0, s0
	s_waitcnt lgkmcnt(0)
	s_barrier
	ds_read_b32 v99, v0
	v_lshl_or_b32 v98, v116, 2, v62
	v_lshlrev_b32_e32 v100, 3, v97
	s_waitcnt lgkmcnt(0)
	v_cmp_lt_i32_e64 s[0:1], v98, v99
	s_and_saveexec_b64 s[2:3], s[0:1]
	s_cbranch_execz .LBB2_171
	s_lshl_b64 s[0:1], s[4:5], 2
	s_add_u32 s4, s68, s0
	s_addc_u32 s5, s69, s1
	s_add_u32 s0, s70, s0
	v_lshlrev_b32_e32 v0, 2, v100
	v_mov_b32_e32 v1, 0
	s_addc_u32 s1, s71, s1
	v_lshl_add_u64 v[88:89], s[4:5], 0, v[0:1]
	v_lshl_add_u64 v[90:91], s[0:1], 0, v[0:1]
	v_lshl_or_b32 v0, v116, 5, v51
	v_add_u32_e32 v0, 0, v0
	v_add_u32_e32 v101, 0x2b00, v0
	v_lshlrev_b32_e32 v0, 1, v62
	v_lshl_or_b32 v0, v116, 3, v0
	v_add_u32_e32 v102, 0, v0
	s_mov_b64 s[4:5], 0
	s_movk_i32 s6, 0x4f
	v_mov_b32_e32 v103, v98
	s_branch .LBB2_169
